# mLSTM chunk loops: 64-lane log-forget scan via DPP row_shr/row_bcast instead of six ds_bpermute round trips
# baseline (speedup 1.0000x reference)
.LBB0_427:
	ds_read_b64 v[46:47], v122
	s_andn2_b64 vcc, exec, s[2:3]
	s_waitcnt lgkmcnt(0)
	s_nop 1
	v_add_f32_dpp v47, v47, v47 row_shr:1 row_mask:0xf bank_mask:0xf
	s_nop 1
	v_add_f32_dpp v47, v47, v47 row_shr:2 row_mask:0xf bank_mask:0xf
	s_nop 1
	v_add_f32_dpp v47, v47, v47 row_shr:4 row_mask:0xf bank_mask:0xf
	s_nop 1
	v_add_f32_dpp v47, v47, v47 row_shr:8 row_mask:0xf bank_mask:0xf
	s_nop 1
	v_add_f32_dpp v47, v47, v47 row_bcast:15 row_mask:0xa bank_mask:0xf
	s_nop 1
	v_add_f32_dpp v47, v47, v47 row_bcast:31 row_mask:0xc bank_mask:0xf
	v_sub_f32_e32 v46, v46, v47
	v_readlane_b32 s15, v47, 63
	s_cbranch_vccnz .LBB0_429
	ds_write2st64_b32 v104, v47, v46 offset1:1

.LBB0_554:
	ds_read_b64 v[44:45], v162
	s_andn2_b64 vcc, exec, s[2:3]
	s_waitcnt lgkmcnt(0)
	s_nop 1
	v_add_f32_dpp v45, v45, v45 row_shr:1 row_mask:0xf bank_mask:0xf
	s_nop 1
	v_add_f32_dpp v45, v45, v45 row_shr:2 row_mask:0xf bank_mask:0xf
	s_nop 1
	v_add_f32_dpp v45, v45, v45 row_shr:4 row_mask:0xf bank_mask:0xf
	s_nop 1
	v_add_f32_dpp v45, v45, v45 row_shr:8 row_mask:0xf bank_mask:0xf
	s_nop 1
	v_add_f32_dpp v45, v45, v45 row_bcast:15 row_mask:0xa bank_mask:0xf
	s_nop 1
	v_add_f32_dpp v45, v45, v45 row_bcast:31 row_mask:0xc bank_mask:0xf
	v_sub_f32_e32 v44, v44, v45
	v_readlane_b32 s33, v45, 63
	s_cbranch_vccnz .LBB0_556
	ds_write2st64_b32 v136, v45, v44 offset1:1
